# GQA plain loop step 1: first 16 exponentials hoisted into the freed slots ahead of the first LDS wait
# baseline (speedup 1.0000x reference)
; DI f32x16 mfma8(v8i a, v8i b, f32x16 c) { return __builtin_amdgcn_mfma_scale_f32_32x32x64_f8f6f4(a, b, c, 0, 0, 0, 0, 0, 0); }
; DI void attn_unit_a8(unsigned char* lds, const AttnArgs& a) {
;     ...
;     auto step = [&](int t, u32x2& kl, u32x2& vl, const u32x2& ks, const u32x2& vs, f32x16& c0, f32x16& c1, f32x16& n0, f32x16& n1, const int hk, const int wj) __attribute__((always_inline)) {
;         const int slot1 = slot == 2 ? 0 : slot + 1, slot2 = slot1 == 2 ? 0 : slot1 + 1;
;         if (hk == 1) { w_cvt(); w_issue(wj + 1 < AT_NWT ? wj + 1 : AT_NWT - 1); }
;         if (hk == 2) w_store(wj);
;         { const int tn = t + 3; gload(tn < a.t1 ? tn : a.t1 - 1, kl, vl); }
;         const unsigned char* Kb = lds + slot * AT_BUFB; const unsigned char* Kn = lds + slot1 * AT_BUFB;
;         const v8i k0 = kread(Kn, 0), k1 = kread(Kn, 1), v0 = vread(Kb, 0), v1 = vread(Kb, 1);
;         n0 = mfma8(k0, qf8, cinit); n1 = mfma8(k1, qf8, cinit);
;         expsum(c0); expsum(c1);
;         const v8i P = pack8(c0, c1);
;         o0[0] = mfma8(v0, P, o0[0]); o0[1] = mfma8(v1, P, o0[1]);
;         lstore(slot2, ks, vs);
;         __syncthreads();
;         slot = slot1;
;     };
.LBB0_714:
	s_min_i32 s4, s56, 64
	s_add_i32 s6, s4, 3
	s_cmp_lt_u32 s56, 61
	s_cselect_b64 s[10:11], -1, 0
	s_lshl_b32 s4, s6, 6
	s_add_i32 s7, s4, 0xfffff000
	s_and_b64 s[12:13], s[10:11], exec
	v_exp_f32_e32 v82, v82
	s_cselect_b32 s4, s4, s7
	v_exp_f32_e32 v83, v83
	v_exp_f32_e32 v86, v86
	v_exp_f32_e32 v87, v87
	v_exp_f32_e32 v90, v90
	v_exp_f32_e32 v91, v91
	v_exp_f32_e32 v94, v94
	v_exp_f32_e32 v95, v95
	v_add_u32_e32 v42, s4, v154
	s_add_i32 s4, s8, 1
	s_cmp_lg_u32 s8, 2
	s_mov_b32 s9, s8
	s_cselect_b32 s8, s4, 0
	s_mul_i32 s4, s8, 0x4680
	v_add_u32_e32 v106, s4, v157
	ds_read_b128 v[34:37], v106
	ds_read_b128 v[38:41], v106 offset:16
	v_exp_f32_e32 v124, v66
	s_and_b64 s[10:11], s[10:11], exec
	v_ashrrev_i32_e32 v43, 31, v42
	v_exp_f32_e32 v125, v67
	v_exp_f32_e32 v146, v70
	v_exp_f32_e32 v147, v71
	v_exp_f32_e32 v74, v74
	v_exp_f32_e32 v75, v75
	v_exp_f32_e32 v78, v78
	v_exp_f32_e32 v79, v79
	s_cselect_b32 s10, s58, s60
	s_cselect_b32 s11, s59, s61
	s_ashr_i32 s7, s6, 31
	s_waitcnt lgkmcnt(0)
	v_mfma_f32_32x32x64_f8f6f4 v[50:65], v[34:41], v[98:105], 0
	v_lshlrev_b64 v[34:35], 7, v[42:43]
	s_lshl_b64 s[12:13], s[6:7], 6
	v_lshl_add_u64 v[34:35], s[10:11], 0, v[34:35]
	v_lshl_add_u64 v[34:35], v[34:35], 0, v[130:131]
	v_lshl_add_u64 v[42:43], v[132:133], 0, s[12:13]
	global_load_dwordx2 v[112:113], v[34:35], off
	ds_read_b128 v[34:37], v106 offset:2560
	ds_read_b128 v[38:41], v106 offset:2576
	global_load_dwordx2 v[114:115], v[42:43], off
	s_mulk_i32 s9, 0x4680
	v_add_u32_e32 v42, s9, v157
	s_nop 0
	s_nop 0
	s_nop 0
	s_nop 0
	s_nop 0
	s_nop 0
	s_nop 0
	s_nop 0
	s_nop 0
	s_nop 0
	s_nop 0
	s_nop 0
	s_nop 0
	s_nop 0
	s_nop 0
	s_nop 0
	ds_read_b128 v[116:119], v42 offset:5120
	ds_read_b128 v[120:123], v42 offset:5136
	ds_read_b128 v[138:141], v42 offset:7680
	ds_read_b128 v[142:145], v42 offset:7696
	v_exp_f32_e32 v84, v84
	v_exp_f32_e32 v85, v85
	v_exp_f32_e32 v88, v88
	v_exp_f32_e32 v89, v89
	v_exp_f32_e32 v92, v92
	v_exp_f32_e32 v93, v93
	v_exp_f32_e32 v96, v96
	v_exp_f32_e32 v97, v97
	v_exp_f32_e32 v126, v68
	v_exp_f32_e32 v127, v69
	v_exp_f32_e32 v148, v72
	v_exp_f32_e32 v149, v73
	v_exp_f32_e32 v76, v76
	v_exp_f32_e32 v77, v77
	v_exp_f32_e32 v80, v80
	v_exp_f32_e32 v81, v81
	s_nop 0
	s_nop 0
	s_nop 0
	s_nop 0
	s_nop 0
	s_nop 0
	s_nop 0
	s_nop 0
	v_cvt_scalef32_pk_fp8_f32 v66, v82, v83, s48
	v_cvt_scalef32_pk_fp8_f32 v70, v124, v125, s48
	v_cvt_scalef32_pk_fp8_f32 v67, v86, v87, s48
	v_cvt_scalef32_pk_fp8_f32 v71, v146, v147, s48
	v_cvt_scalef32_pk_fp8_f32 v68, v90, v91, s48
	v_cvt_scalef32_pk_fp8_f32 v72, v74, v75, s48
	v_cvt_scalef32_pk_fp8_f32 v69, v94, v95, s48
	v_cvt_scalef32_pk_fp8_f32 v73, v78, v79, s48
	v_cvt_scalef32_pk_fp8_f32 v66, v84, v85, s48 op_sel:[0,0,0,1]
	v_cvt_scalef32_pk_fp8_f32 v70, v126, v127, s48 op_sel:[0,0,0,1]
	v_cvt_scalef32_pk_fp8_f32 v67, v88, v89, s48 op_sel:[0,0,0,1]
	v_cvt_scalef32_pk_fp8_f32 v71, v148, v149, s48 op_sel:[0,0,0,1]
	v_cvt_scalef32_pk_fp8_f32 v68, v92, v93, s48 op_sel:[0,0,0,1]
	v_cvt_scalef32_pk_fp8_f32 v72, v76, v77, s48 op_sel:[0,0,0,1]
	v_cvt_scalef32_pk_fp8_f32 v69, v96, v97, s48 op_sel:[0,0,0,1]
	v_cvt_scalef32_pk_fp8_f32 v73, v80, v81, s48 op_sel:[0,0,0,1]
	s_waitcnt lgkmcnt(4)
	v_mfma_f32_32x32x64_f8f6f4 v[34:49], v[34:41], v[98:105], 0
	s_addk_i32 s4, 0x4680
	s_cmp_eq_u32 s8, 2
	v_add_f32_e64 v110, v110, v84
	v_add_f32_e64 v111, v111, v85
	v_add_f32_e64 v82, v108, v82
	v_add_f32_e64 v83, v109, v83
	s_cselect_b64 s[6:7], -1, 0
	v_add_f32_e64 v84, v88, v110
	v_add_f32_e64 v85, v89, v111
	v_add_f32_e64 v82, v86, v82
	v_add_f32_e64 v83, v87, v83
	v_add_f32_e64 v84, v92, v84
	v_add_f32_e64 v85, v93, v85
	v_pk_add_f32 v[82:83], v[90:91], v[82:83]
	s_and_b64 s[10:11], s[6:7], exec
	v_pk_add_f32 v[84:85], v[96:97], v[84:85]
	v_pk_add_f32 v[82:83], v[94:95], v[82:83]
	s_cselect_b32 s4, 0, s4
	v_pk_add_f32 v[82:83], v[124:125], v[82:83]
	v_pk_add_f32 v[84:85], v[126:127], v[84:85]
	s_waitcnt lgkmcnt(2)
	v_mfma_f32_32x32x64_f8f6f4 v[18:33], v[116:123], v[66:73], v[18:33]
	s_add_i32 s4, s4, 0
	v_add_f32_e64 v84, v148, v84
	v_add_f32_e64 v85, v149, v85
	v_add_f32_e64 v82, v146, v82
	v_add_f32_e64 v83, v147, v83
	v_add_f32_e64 v76, v76, v84
	v_add_f32_e64 v77, v77, v85
	v_add_f32_e64 v74, v74, v82
	v_add_f32_e64 v75, v75, v83
	v_add_f32_e64 v110, v80, v76
	v_add_f32_e64 v111, v81, v77
	v_add_f32_e64 v108, v78, v74
	v_add_f32_e64 v109, v79, v75
	s_cmpk_gt_u32 s56, 0x42
	s_waitcnt lgkmcnt(0)
	v_mfma_f32_32x32x64_f8f6f4 v[2:17], v[138:145], v[66:73], v[2:17]
	v_add_u32_e32 v66, s4, v155
	s_waitcnt vmcnt(3)
	ds_write_b64 v66, v[134:135]
	v_add_u32_e32 v66, s4, v156
	v_add_u32_e32 v66, 0x1400, v66
	s_waitcnt vmcnt(2)
	ds_write2_b32 v66, v136, v137 offset1:8
	s_waitcnt lgkmcnt(0)
	s_barrier
; DI f32x16 mfma8(v8i a, v8i b, f32x16 c) { return __builtin_amdgcn_mfma_scale_f32_32x32x64_f8f6f4(a, b, c, 0, 0, 0, 0, 0, 0); }
; DI void attn_unit_a8(unsigned char* lds, const AttnArgs& a) {
;     ...
;     auto step = [&](int t, u32x2& kl, u32x2& vl, const u32x2& ks, const u32x2& vs, f32x16& c0, f32x16& c1, f32x16& n0, f32x16& n1, const int hk, const int wj) __attribute__((always_inline)) {
;         const int slot1 = slot == 2 ? 0 : slot + 1, slot2 = slot1 == 2 ? 0 : slot1 + 1;
;         if (hk == 1) { w_cvt(); w_issue(wj + 1 < AT_NWT ? wj + 1 : AT_NWT - 1); }
;         if (hk == 2) w_store(wj);
;         { const int tn = t + 3; gload(tn < a.t1 ? tn : a.t1 - 1, kl, vl); }
;         const unsigned char* Kb = lds + slot * AT_BUFB; const unsigned char* Kn = lds + slot1 * AT_BUFB;
;         const v8i k0 = kread(Kn, 0), k1 = kread(Kn, 1), v0 = vread(Kb, 0), v1 = vread(Kb, 1);
;         n0 = mfma8(k0, qf8, cinit); n1 = mfma8(k1, qf8, cinit);
;         expsum(c0); expsum(c1);
;         const v8i P = pack8(c0, c1);
;         o0[0] = mfma8(v0, P, o0[0]); o0[1] = mfma8(v1, P, o0[1]);
;         lstore(slot2, ks, vs);
;         __syncthreads();
;         slot = slot1;
;     };
	s_cbranch_scc1 .LBB0_716
	s_min_u32 s4, s56, 63
	s_cmp_lt_u32 s56, 60
	s_cselect_b64 s[10:11], -1, 0
	s_lshl_b32 s4, s4, 6
	s_add_i32 s9, s4, 0x100
	s_add_i32 s14, s4, 0xfffff100
	s_and_b64 s[12:13], s[10:11], exec
	s_cselect_b32 s9, s9, s14
	s_add_i32 s8, s8, 1
	s_and_b64 s[6:7], s[6:7], exec
	v_add_u32_e32 v82, s9, v154
	s_cselect_b32 s8, 0, s8
	s_and_b64 s[10:11], s[10:11], exec
	v_ashrrev_i32_e32 v83, 31, v82
	s_cselect_b32 s11, s59, s61
	s_cselect_b32 s10, s58, s60
	v_lshlrev_b64 v[82:83], 7, v[82:83]
	s_mul_i32 s6, s8, 0x4680
	v_lshl_add_u64 v[90:91], s[10:11], 0, v[82:83]
	v_add_u32_e32 v86, s6, v157
	v_lshl_add_u64 v[90:91], v[90:91], 0, v[130:131]
	ds_read_b128 v[66:69], v86 offset:2560
	ds_read_b128 v[70:73], v86 offset:2576
	ds_read_b128 v[82:85], v86
	ds_read_b128 v[86:89], v86 offset:16
	global_load_dwordx2 v[134:135], v[90:91], off
	v_lshl_add_u64 v[90:91], v[132:133], 0, s[4:5]
	global_load_dwordx2 v[136:137], v[90:91], off offset:256
	v_exp_f32_e32 v50, v50
	v_exp_f32_e32 v51, v51
	v_exp_f32_e32 v54, v54
	v_exp_f32_e32 v55, v55
	v_exp_f32_e32 v58, v58
	v_exp_f32_e32 v59, v59
	v_exp_f32_e32 v62, v62
	v_exp_f32_e32 v63, v63
	v_exp_f32_e32 v124, v34
	v_exp_f32_e32 v125, v35
	v_exp_f32_e32 v146, v38
	v_exp_f32_e32 v147, v39
	v_exp_f32_e32 v42, v42
	v_exp_f32_e32 v43, v43
	v_exp_f32_e32 v46, v46
	v_exp_f32_e32 v47, v47
	ds_read_b128 v[116:119], v106 offset:5120
	ds_read_b128 v[120:123], v106 offset:5136
	ds_read_b128 v[138:141], v106 offset:7680
	ds_read_b128 v[142:145], v106 offset:7696
	v_exp_f32_e32 v52, v52
	v_exp_f32_e32 v53, v53
	v_exp_f32_e32 v56, v56
	v_exp_f32_e32 v57, v57
	v_exp_f32_e32 v60, v60
	v_exp_f32_e32 v61, v61
	v_exp_f32_e32 v64, v64
	v_exp_f32_e32 v65, v65
	v_exp_f32_e32 v126, v36
	v_exp_f32_e32 v127, v37
	v_exp_f32_e32 v148, v40
	v_exp_f32_e32 v149, v41
	v_exp_f32_e32 v44, v44
	v_exp_f32_e32 v45, v45
	v_exp_f32_e32 v48, v48
	v_exp_f32_e32 v49, v49
	s_nop 0
	s_nop 0
	s_nop 0
	s_nop 0
	s_nop 0
	s_nop 0
	s_nop 0
	s_nop 0
	s_waitcnt lgkmcnt(6)
	v_mfma_f32_32x32x64_f8f6f4 v[66:81], v[66:73], v[98:105], 0
	v_cvt_scalef32_pk_fp8_f32 v34, v50, v51, s48
	v_cvt_scalef32_pk_fp8_f32 v38, v124, v125, s48
	v_cvt_scalef32_pk_fp8_f32 v35, v54, v55, s48
	v_cvt_scalef32_pk_fp8_f32 v39, v146, v147, s48
	v_cvt_scalef32_pk_fp8_f32 v36, v58, v59, s48
	v_cvt_scalef32_pk_fp8_f32 v40, v42, v43, s48
	v_cvt_scalef32_pk_fp8_f32 v37, v62, v63, s48
	v_cvt_scalef32_pk_fp8_f32 v41, v46, v47, s48
	v_cvt_scalef32_pk_fp8_f32 v34, v52, v53, s48 op_sel:[0,0,0,1]
	v_cvt_scalef32_pk_fp8_f32 v38, v126, v127, s48 op_sel:[0,0,0,1]
	v_cvt_scalef32_pk_fp8_f32 v35, v56, v57, s48 op_sel:[0,0,0,1]
	v_cvt_scalef32_pk_fp8_f32 v39, v148, v149, s48 op_sel:[0,0,0,1]
	v_cvt_scalef32_pk_fp8_f32 v36, v60, v61, s48 op_sel:[0,0,0,1]
	v_cvt_scalef32_pk_fp8_f32 v40, v44, v45, s48 op_sel:[0,0,0,1]
	v_cvt_scalef32_pk_fp8_f32 v37, v64, v65, s48 op_sel:[0,0,0,1]
	s_waitcnt lgkmcnt(4)
	v_mfma_f32_32x32x64_f8f6f4 v[82:97], v[82:89], v[98:105], 0
	v_cvt_scalef32_pk_fp8_f32 v41, v48, v49, s48 op_sel:[0,0,0,1]
	v_add_f32_e64 v110, v110, v52
	v_add_f32_e64 v111, v111, v53
	v_add_f32_e64 v50, v108, v50
	v_add_f32_e64 v51, v109, v51
	s_addk_i32 s6, 0x4680
	v_add_f32_e64 v52, v56, v110
	v_add_f32_e64 v53, v57, v111
	v_add_f32_e64 v50, v54, v50
	v_add_f32_e64 v51, v55, v51
	s_cmp_lg_u32 s8, 2
	v_add_f32_e64 v50, v58, v50
	v_add_f32_e64 v51, v59, v51
	v_pk_add_f32 v[52:53], v[60:61], v[52:53]
	s_cselect_b32 s4, s6, 0
	v_pk_add_f32 v[52:53], v[64:65], v[52:53]
	v_pk_add_f32 v[50:51], v[62:63], v[50:51]
	s_add_i32 s4, s4, 0
	v_pk_add_f32 v[50:51], v[124:125], v[50:51]
	v_pk_add_f32 v[52:53], v[126:127], v[52:53]
	s_waitcnt lgkmcnt(2)
	v_mfma_f32_32x32x64_f8f6f4 v[18:33], v[116:123], v[34:41], v[18:33]
	v_add_f32_e64 v52, v148, v52
	v_add_f32_e64 v53, v149, v53
	v_add_f32_e64 v50, v146, v50
	v_add_f32_e64 v51, v147, v51
	v_add_f32_e64 v44, v44, v52
	v_add_f32_e64 v45, v45, v53
	v_add_f32_e64 v42, v42, v50
	v_add_f32_e64 v43, v43, v51
	v_add_f32_e64 v110, v48, v44
	v_add_f32_e64 v111, v49, v45
	v_add_f32_e64 v108, v46, v42
	v_add_f32_e64 v109, v47, v43
	s_nop 0
	s_nop 0
	s_nop 0
	s_nop 0
	s_nop 0
	s_nop 0
	s_nop 0
	s_nop 0
	s_waitcnt lgkmcnt(0)
	v_mfma_f32_32x32x64_f8f6f4 v[2:17], v[138:145], v[34:41], v[2:17]
	v_add_u32_e32 v34, s4, v155
	s_waitcnt vmcnt(3)
	ds_write_b64 v34, v[112:113]
	v_add_u32_e32 v34, s4, v156
	v_add_u32_e32 v34, 0x1400, v34
	s_waitcnt vmcnt(2)
	ds_write2_b32 v34, v114, v115 offset1:8
	s_nop 0
	s_nop 0
	s_nop 0
	s_nop 0
	s_nop 0
	s_nop 0
	s_nop 0
	s_nop 0
	s_waitcnt lgkmcnt(0)
	s_barrier

; DI void attn_unit_a8(unsigned char* lds, const AttnArgs& a) {
;     ...
;     auto expsum = [&](f32x16& sc) __attribute__((always_inline)) {
; #pragma unroll
;         for (int i = 0; i < 16; ++i) sc[i] = __builtin_amdgcn_exp2f(sc[i]);
; #pragma unroll
;         for (int i = 0; i < 4; ++i) l0 += (f32x4){sc[4 * i], sc[4 * i + 1], sc[4 * i + 2], sc[4 * i + 3]};
;     };
;     auto pack8 = [&](const f32x16& s0, const f32x16& s1) __attribute__((always_inline)) -> v8i { v8i p;
; #pragma unroll
;         for (int g = 0; g < 4; ++g) { p[g] = (int)pk4_fp8_div16(s0[4 * g], s0[4 * g + 1], s0[4 * g + 2], s0[4 * g + 3]); p[4 + g] = (int)pk4_fp8_div16(s1[4 * g], s1[4 * g + 1], s1[4 * g + 2], s1[4 * g + 3]); }
;         return p; };
;     f32x4 wq[4];
;     const int wn4 = (tid & 63) * 4;
;     constexpr int WPITCH = 36;
;     auto w_decode = [&](int j, const float*& src, unsigned char*& dst, int& ld, int& n0, int& k0, bool& gu) __attribute__((always_inline)) {
;         const int g = (j >> 2) * 512 + a.wl, e = g / 96, rr = g - e * 96; KParamsPtr kp = kparams();
;         if (rr < 64) { src = kp->w_gu + ((size_t)a.wli * NE + e) * (1024 * 2048); dst = kp->ws + WS_WGU + (size_t)a.wli * SZ_WGU + (size_t)e * 2048 * 1024; ld = 2048; n0 = (rr & 7) * 256; k0 = ((rr >> 3) * 4 + (j & 3)) * 32; gu = true; }
;         else { const int q = rr - 64; src = kp->w_dn + ((size_t)a.wli * NE + e) * (1024 * 1024); dst = kp->ws + WS_WDN + (size_t)a.wli * SZ_WDN + (size_t)e * 1024 * 1024; ld = 1024; n0 = (q & 3) * 256; k0 = ((q >> 2) * 4 + (j & 3)) * 32; gu = false; } };
;     auto w_issue = [&](int j) __attribute__((always_inline)) { const float* src; unsigned char* dst; int ld, n0, k0; bool gu; w_decode(j, src, dst, ld, n0, k0, gu);
;         const float* p = src + (size_t)(k0 + 4 * wid) * ld + n0 + wn4;
;         wq[0] = __builtin_nontemporal_load((const f32x4*)p); wq[1] = __builtin_nontemporal_load((const f32x4*)(p + ld));
;         wq[2] = __builtin_nontemporal_load((const f32x4*)(p + (size_t)2 * ld)); wq[3] = __builtin_nontemporal_load((const f32x4*)(p + (size_t)3 * ld)); };
;     auto w_cvt = [&]() __attribute__((always_inline)) { unsigned char* t8 = lds + AT_WT + wn4 * WPITCH + 4 * wid;
; #pragma unroll
;         for (int j = 0; j < 4; ++j) *(unsigned*)(t8 + j * WPITCH) = pk4_fp8_mul64(wq[0][j], wq[1][j], wq[2][j], wq[3][j]); };
;     const int wcol = tid >> 1, whalf = tid & 1;
.LBB0_1934:
	s_min_u32 s8, s50, 64
	s_cmp_lt_u32 s50, 61
	s_cselect_b64 s[10:11], -1, 0
	s_lshl_b32 s8, s8, 6
	s_add_i32 s15, s8, 0xc0
	s_add_i32 s18, s8, 0xfffff0c0
	s_and_b64 s[16:17], s[10:11], exec
	s_cselect_b32 s15, s15, s18
	s_mov_b32 s18, s14
	s_add_i32 s14, s14, 1
	s_cmp_lg_u32 s18, 2
	s_cselect_b32 s14, s14, 0
	s_mul_i32 s19, s14, 0x4680
	v_exp_f32_e32 v82, v82
	v_add_u32_e32 v106, s19, v169
	v_exp_f32_e32 v83, v83
	v_exp_f32_e32 v86, v86
	v_exp_f32_e32 v87, v87
	v_exp_f32_e32 v90, v90
	v_exp_f32_e32 v91, v91
	v_exp_f32_e32 v94, v94
	v_exp_f32_e32 v95, v95
	ds_read_b128 v[50:53], v106
	ds_read_b128 v[54:57], v106 offset:16
	v_add_u32_e32 v58, s15, v130
	v_exp_f32_e32 v124, v66
	s_and_b64 s[10:11], s[10:11], exec
	v_ashrrev_i32_e32 v59, 31, v58
	v_exp_f32_e32 v125, v67
	v_exp_f32_e32 v148, v70
	v_exp_f32_e32 v149, v71
	v_exp_f32_e32 v74, v74
	v_exp_f32_e32 v75, v75
	v_exp_f32_e32 v78, v78
	v_exp_f32_e32 v79, v79
	s_cselect_b32 s16, s42, s12
	s_cselect_b32 s17, s43, s13
	s_waitcnt lgkmcnt(0)
	v_mfma_f32_32x32x64_f8f6f4 v[34:49], v[50:57], v[98:105], 0
	v_lshlrev_b64 v[50:51], 7, v[58:59]
	v_lshl_add_u64 v[50:51], s[16:17], 0, v[50:51]
	v_lshl_add_u64 v[50:51], v[50:51], 0, v[132:133]
	v_lshl_add_u64 v[58:59], v[134:135], 0, s[8:9]
	global_load_dwordx2 v[112:113], v[50:51], off
	ds_read_b128 v[50:53], v106 offset:2560
	ds_read_b128 v[54:57], v106 offset:2576
	global_load_dwordx2 v[114:115], v[58:59], off offset:192
	s_mulk_i32 s18, 0x4680
	v_add_u32_e32 v58, s18, v169
	s_nop 0
	s_nop 0
	s_nop 0
	s_nop 0
	s_nop 0
	s_nop 0
	s_nop 0
	s_nop 0
	s_nop 0
	s_nop 0
	s_nop 0
	s_nop 0
	s_nop 0
	s_nop 0
	s_nop 0
	s_nop 0
	ds_read_b128 v[116:119], v58 offset:5120
	ds_read_b128 v[120:123], v58 offset:5136
	ds_read_b128 v[140:143], v58 offset:7680
	ds_read_b128 v[144:147], v58 offset:7696
	v_exp_f32_e32 v84, v84
	v_exp_f32_e32 v85, v85
	v_exp_f32_e32 v88, v88
	v_exp_f32_e32 v89, v89
	v_exp_f32_e32 v92, v92
	v_exp_f32_e32 v93, v93
	v_exp_f32_e32 v96, v96
	v_exp_f32_e32 v97, v97
	v_exp_f32_e32 v126, v68
	v_exp_f32_e32 v127, v69
	v_exp_f32_e32 v150, v72
	v_exp_f32_e32 v151, v73
	v_exp_f32_e32 v76, v76
	v_exp_f32_e32 v77, v77
	v_exp_f32_e32 v80, v80
	v_exp_f32_e32 v81, v81
	s_nop 0
	s_nop 0
	s_nop 0
	s_nop 0
	s_nop 0
	s_nop 0
	s_nop 0
	s_nop 0
	v_cvt_scalef32_pk_fp8_f32 v66, v82, v83, s69
	v_cvt_scalef32_pk_fp8_f32 v70, v124, v125, s69
	v_cvt_scalef32_pk_fp8_f32 v67, v86, v87, s69
	v_cvt_scalef32_pk_fp8_f32 v71, v148, v149, s69
	v_cvt_scalef32_pk_fp8_f32 v68, v90, v91, s69
	v_cvt_scalef32_pk_fp8_f32 v72, v74, v75, s69
	v_cvt_scalef32_pk_fp8_f32 v69, v94, v95, s69
	v_cvt_scalef32_pk_fp8_f32 v73, v78, v79, s69
	v_cvt_scalef32_pk_fp8_f32 v66, v84, v85, s69 op_sel:[0,0,0,1]
	v_cvt_scalef32_pk_fp8_f32 v70, v126, v127, s69 op_sel:[0,0,0,1]
	v_cvt_scalef32_pk_fp8_f32 v67, v88, v89, s69 op_sel:[0,0,0,1]
	v_cvt_scalef32_pk_fp8_f32 v71, v150, v151, s69 op_sel:[0,0,0,1]
	v_cvt_scalef32_pk_fp8_f32 v68, v92, v93, s69 op_sel:[0,0,0,1]
	v_cvt_scalef32_pk_fp8_f32 v72, v76, v77, s69 op_sel:[0,0,0,1]
	v_cvt_scalef32_pk_fp8_f32 v69, v96, v97, s69 op_sel:[0,0,0,1]
	v_cvt_scalef32_pk_fp8_f32 v73, v80, v81, s69 op_sel:[0,0,0,1]
	s_waitcnt lgkmcnt(4)
	v_mfma_f32_32x32x64_f8f6f4 v[50:65], v[50:57], v[98:105], 0
	s_add_i32 s15, s19, 0x4680
	s_cmp_eq_u32 s14, 2
	v_add_f32_e64 v110, v110, v84
	v_add_f32_e64 v111, v111, v85
	v_add_f32_e64 v82, v108, v82
	v_add_f32_e64 v83, v109, v83
	s_cselect_b64 s[10:11], -1, 0
	v_add_f32_e64 v84, v88, v110
	v_add_f32_e64 v85, v89, v111
	v_add_f32_e64 v82, v86, v82
	v_add_f32_e64 v83, v87, v83
	v_add_f32_e64 v84, v92, v84
	v_add_f32_e64 v85, v93, v85
	v_pk_add_f32 v[82:83], v[90:91], v[82:83]
	s_and_b64 s[16:17], s[10:11], exec
	v_pk_add_f32 v[84:85], v[96:97], v[84:85]
	v_pk_add_f32 v[82:83], v[94:95], v[82:83]
	s_cselect_b32 s8, 0, s15
	v_pk_add_f32 v[82:83], v[124:125], v[82:83]
	v_pk_add_f32 v[84:85], v[126:127], v[84:85]
	s_waitcnt lgkmcnt(2)
	v_mfma_f32_32x32x64_f8f6f4 v[18:33], v[116:123], v[66:73], v[18:33]
	s_add_i32 s8, s8, 0
	v_add_f32_e64 v84, v150, v84
	v_add_f32_e64 v85, v151, v85
	v_add_f32_e64 v82, v148, v82
	v_add_f32_e64 v83, v149, v83
	v_add_f32_e64 v76, v76, v84
	v_add_f32_e64 v77, v77, v85
	v_add_f32_e64 v74, v74, v82
	v_add_f32_e64 v75, v75, v83
	v_add_f32_e64 v110, v80, v76
	v_add_f32_e64 v111, v81, v77
	v_add_f32_e64 v108, v78, v74
	v_add_f32_e64 v109, v79, v75
	s_cmpk_gt_u32 s50, 0x42
	s_waitcnt lgkmcnt(0)
	v_mfma_f32_32x32x64_f8f6f4 v[2:17], v[140:147], v[66:73], v[2:17]
	v_add_u32_e32 v66, s8, v131
	s_waitcnt vmcnt(3)
	ds_write_b64 v66, v[136:137]
	v_add_u32_e32 v66, s8, v168
	v_add_u32_e32 v66, 0x1400, v66
	s_waitcnt vmcnt(2)
	ds_write2_b32 v66, v138, v139 offset1:8
	s_waitcnt lgkmcnt(0)
	s_barrier
; DI void attn_unit_a8(unsigned char* lds, const AttnArgs& a) {
;     ...
;     auto expsum = [&](f32x16& sc) __attribute__((always_inline)) {
; #pragma unroll
;         for (int i = 0; i < 16; ++i) sc[i] = __builtin_amdgcn_exp2f(sc[i]);
; #pragma unroll
;         for (int i = 0; i < 4; ++i) l0 += (f32x4){sc[4 * i], sc[4 * i + 1], sc[4 * i + 2], sc[4 * i + 3]};
;     };
;     auto pack8 = [&](const f32x16& s0, const f32x16& s1) __attribute__((always_inline)) -> v8i { v8i p;
; #pragma unroll
;         for (int g = 0; g < 4; ++g) { p[g] = (int)pk4_fp8_div16(s0[4 * g], s0[4 * g + 1], s0[4 * g + 2], s0[4 * g + 3]); p[4 + g] = (int)pk4_fp8_div16(s1[4 * g], s1[4 * g + 1], s1[4 * g + 2], s1[4 * g + 3]); }
;         return p; };
;     f32x4 wq[4];
;     const int wn4 = (tid & 63) * 4;
;     constexpr int WPITCH = 36;
;     auto w_decode = [&](int j, const float*& src, unsigned char*& dst, int& ld, int& n0, int& k0, bool& gu) __attribute__((always_inline)) {
;         const int g = (j >> 2) * 512 + a.wl, e = g / 96, rr = g - e * 96; KParamsPtr kp = kparams();
;         if (rr < 64) { src = kp->w_gu + ((size_t)a.wli * NE + e) * (1024 * 2048); dst = kp->ws + WS_WGU + (size_t)a.wli * SZ_WGU + (size_t)e * 2048 * 1024; ld = 2048; n0 = (rr & 7) * 256; k0 = ((rr >> 3) * 4 + (j & 3)) * 32; gu = true; }
;         else { const int q = rr - 64; src = kp->w_dn + ((size_t)a.wli * NE + e) * (1024 * 1024); dst = kp->ws + WS_WDN + (size_t)a.wli * SZ_WDN + (size_t)e * 1024 * 1024; ld = 1024; n0 = (q & 3) * 256; k0 = ((q >> 2) * 4 + (j & 3)) * 32; gu = false; } };
;     auto w_issue = [&](int j) __attribute__((always_inline)) { const float* src; unsigned char* dst; int ld, n0, k0; bool gu; w_decode(j, src, dst, ld, n0, k0, gu);
;         const float* p = src + (size_t)(k0 + 4 * wid) * ld + n0 + wn4;
;         wq[0] = __builtin_nontemporal_load((const f32x4*)p); wq[1] = __builtin_nontemporal_load((const f32x4*)(p + ld));
;         wq[2] = __builtin_nontemporal_load((const f32x4*)(p + (size_t)2 * ld)); wq[3] = __builtin_nontemporal_load((const f32x4*)(p + (size_t)3 * ld)); };
;     auto w_cvt = [&]() __attribute__((always_inline)) { unsigned char* t8 = lds + AT_WT + wn4 * WPITCH + 4 * wid;
; #pragma unroll
;         for (int j = 0; j < 4; ++j) *(unsigned*)(t8 + j * WPITCH) = pk4_fp8_mul64(wq[0][j], wq[1][j], wq[2][j], wq[3][j]); };
;     const int wcol = tid >> 1, whalf = tid & 1;
	s_cbranch_scc1 .LBB0_1936
	s_min_u32 s8, s50, 63
	s_cmp_lt_u32 s50, 60
	s_cselect_b64 s[16:17], -1, 0
	s_lshl_b32 s8, s8, 6
	s_add_i32 s15, s8, 0x100
	s_add_i32 s20, s8, 0xfffff100
	s_and_b64 s[18:19], s[16:17], exec
	s_cselect_b32 s15, s15, s20
	s_add_i32 s14, s14, 1
	s_and_b64 s[10:11], s[10:11], exec
	v_add_u32_e32 v82, s15, v130
	s_cselect_b32 s14, 0, s14
	s_and_b64 s[16:17], s[16:17], exec
	v_ashrrev_i32_e32 v83, 31, v82
	s_cselect_b32 s17, s43, s13
	s_cselect_b32 s16, s42, s12
	v_lshlrev_b64 v[82:83], 7, v[82:83]
	s_mul_i32 s10, s14, 0x4680
	v_lshl_add_u64 v[90:91], s[16:17], 0, v[82:83]
	v_add_u32_e32 v86, s10, v169
	v_lshl_add_u64 v[90:91], v[90:91], 0, v[132:133]
	ds_read_b128 v[66:69], v86 offset:2560
	ds_read_b128 v[70:73], v86 offset:2576
	ds_read_b128 v[82:85], v86
	ds_read_b128 v[86:89], v86 offset:16
	global_load_dwordx2 v[136:137], v[90:91], off
	v_lshl_add_u64 v[90:91], v[134:135], 0, s[8:9]
	global_load_dwordx2 v[138:139], v[90:91], off offset:256
	v_exp_f32_e32 v124, v34
	v_exp_f32_e32 v125, v35
	v_exp_f32_e32 v36, v36
	v_exp_f32_e32 v37, v37
	v_exp_f32_e32 v126, v38
	v_exp_f32_e32 v127, v39
	v_exp_f32_e32 v42, v42
	v_exp_f32_e32 v43, v43
	v_exp_f32_e32 v46, v46
	v_exp_f32_e32 v47, v47
	v_exp_f32_e32 v50, v50
	v_exp_f32_e32 v51, v51
	v_exp_f32_e32 v54, v54
	v_exp_f32_e32 v55, v55
	v_exp_f32_e32 v58, v58
	v_exp_f32_e32 v59, v59
	v_exp_f32_e32 v62, v62
	v_exp_f32_e32 v63, v63
	ds_read_b128 v[116:119], v106 offset:5120
	ds_read_b128 v[120:123], v106 offset:5136
	ds_read_b128 v[140:143], v106 offset:7680
	ds_read_b128 v[144:147], v106 offset:7696
	v_exp_f32_e32 v148, v40
	v_exp_f32_e32 v149, v41
	v_exp_f32_e32 v44, v44
	v_exp_f32_e32 v45, v45
	v_exp_f32_e32 v48, v48
	v_exp_f32_e32 v49, v49
	v_exp_f32_e32 v52, v52
	v_exp_f32_e32 v53, v53
	v_exp_f32_e32 v56, v56
	v_exp_f32_e32 v57, v57
	v_exp_f32_e32 v60, v60
	v_exp_f32_e32 v61, v61
	v_exp_f32_e32 v64, v64
	v_exp_f32_e32 v65, v65
	s_nop 0
	v_cvt_scalef32_pk_fp8_f32 v34, v124, v125, s69
	v_pk_add_f32 v[110:111], v[110:111], v[36:37]
	v_cvt_scalef32_pk_fp8_f32 v34, v36, v37, s69 op_sel:[0,0,0,1]
	s_nop 0
	s_nop 0
	s_nop 0
	s_nop 0
	s_nop 0
	s_nop 0
	s_nop 0
	s_waitcnt lgkmcnt(6)
	v_mfma_f32_32x32x64_f8f6f4 v[66:81], v[66:73], v[98:105], 0
	v_cvt_scalef32_pk_fp8_f32 v38, v50, v51, s69
	v_cvt_scalef32_pk_fp8_f32 v35, v126, v127, s69
	v_cvt_scalef32_pk_fp8_f32 v39, v54, v55, s69
	v_cvt_scalef32_pk_fp8_f32 v36, v42, v43, s69
	v_cvt_scalef32_pk_fp8_f32 v40, v58, v59, s69
	v_cvt_scalef32_pk_fp8_f32 v37, v46, v47, s69
	v_cvt_scalef32_pk_fp8_f32 v41, v62, v63, s69
	v_cvt_scalef32_pk_fp8_f32 v38, v52, v53, s69 op_sel:[0,0,0,1]
	v_cvt_scalef32_pk_fp8_f32 v35, v148, v149, s69 op_sel:[0,0,0,1]
	v_cvt_scalef32_pk_fp8_f32 v39, v56, v57, s69 op_sel:[0,0,0,1]
	v_cvt_scalef32_pk_fp8_f32 v36, v44, v45, s69 op_sel:[0,0,0,1]
	v_cvt_scalef32_pk_fp8_f32 v40, v60, v61, s69 op_sel:[0,0,0,1]
	v_cvt_scalef32_pk_fp8_f32 v37, v48, v49, s69 op_sel:[0,0,0,1]
	v_cvt_scalef32_pk_fp8_f32 v41, v64, v65, s69 op_sel:[0,0,0,1]
	v_pk_add_f32 v[108:109], v[108:109], v[124:125]
	s_waitcnt lgkmcnt(4)
	v_mfma_f32_32x32x64_f8f6f4 v[82:97], v[82:89], v[98:105], 0
	s_addk_i32 s10, 0x4680
	v_add_f32_e64 v110, v148, v110
	v_add_f32_e64 v111, v149, v111
	v_add_f32_e64 v108, v126, v108
	v_add_f32_e64 v109, v127, v109
	s_cmp_lg_u32 s14, 2
	v_add_f32_e64 v42, v42, v108
	v_add_f32_e64 v43, v43, v109
	v_add_f32_e64 v44, v44, v110
	v_add_f32_e64 v45, v45, v111
	s_cselect_b32 s8, s10, 0
	v_add_f32_e64 v44, v48, v44
	v_add_f32_e64 v45, v49, v45
	v_pk_add_f32 v[42:43], v[46:47], v[42:43]
	s_add_i32 s8, s8, 0
	v_pk_add_f32 v[42:43], v[50:51], v[42:43]
	v_pk_add_f32 v[44:45], v[52:53], v[44:45]
	v_pk_add_f32 v[42:43], v[54:55], v[42:43]
	v_pk_add_f32 v[44:45], v[56:57], v[44:45]
	v_pk_add_f32 v[42:43], v[58:59], v[42:43]
	s_waitcnt lgkmcnt(2)
	v_mfma_f32_32x32x64_f8f6f4 v[18:33], v[116:123], v[34:41], v[18:33]
	v_add_f32_e64 v44, v60, v44
	v_add_f32_e64 v45, v61, v45
	v_add_f32_e64 v108, v62, v42
	v_add_f32_e64 v109, v63, v43
	v_add_f32_e64 v110, v64, v44
	v_add_f32_e64 v111, v65, v45
	s_nop 0
	s_nop 0
	s_nop 0
	s_nop 0
	s_nop 0
	s_nop 0
	s_nop 0
	s_nop 0
	s_waitcnt lgkmcnt(0)
	v_mfma_f32_32x32x64_f8f6f4 v[2:17], v[140:147], v[34:41], v[2:17]
	v_add_u32_e32 v34, s8, v131
	s_waitcnt vmcnt(3)
	ds_write_b64 v34, v[112:113]
	v_add_u32_e32 v34, s8, v168
	v_add_u32_e32 v34, 0x1400, v34
	s_waitcnt vmcnt(2)
	ds_write2_b32 v34, v114, v115 offset1:8
	s_nop 0
	s_nop 0
	s_nop 0
	s_nop 0
	s_nop 0
	s_nop 0
	s_nop 0
	s_nop 0
	s_waitcnt lgkmcnt(0)
	s_barrier
